# prepw
# speedup vs baseline: 1.1251x; 1.0046x over previous
.LBB0_44:
	v_lshl_or_b32 v7, s2, 8, v0
	v_and_b32_e32 v2, 31, v0
	v_bfe_u32 v3, v0, 5, 1
	s_cmp_lt_u32 s2, 12
	s_cbranch_scc1 .Lw1f8
	v_lshrrev_b32_e32 v1, 6, v7
	s_cmp_lt_u32 s2, 20
	v_readfirstlane_b32 s10, v1
	s_cbranch_scc1 .Lw2bf
	s_load_dwordx2 s[12:13], s[0:1], 0x20
	s_sub_u32 s10, s10, 0x50
	s_mul_i32 s10, s10, 0xc0
	v_mul_u32_u24_e32 v4, 48, v3
	v_lshl_add_u32 v4, v2, 2, v4
	v_add_u32_e32 v4, s10, v4
	v_add_u32_e32 v5, 0xffffec00, v7
	v_lshlrev_b32_e32 v5, 4, v5
	v_add_u32_e32 v5, 0x14000, v5
	v_mov_b32_e32 v16, 0
	v_mov_b32_e32 v17, 0
	v_mov_b32_e32 v18, 0
	v_mov_b32_e32 v19, 0
	v_mov_b32_e32 v20, 0
	v_mov_b32_e32 v21, 0
	v_mov_b32_e32 v22, 0
	v_mov_b32_e32 v23, 0
	v_cmp_gt_u32_e32 vcc, 3, v2
	s_and_saveexec_b64 s[14:15], vcc
	s_waitcnt lgkmcnt(0)
	global_load_dword v16, v4, s[12:13] offset:0
	global_load_dword v17, v4, s[12:13] offset:12
	global_load_dword v18, v4, s[12:13] offset:24
	global_load_dword v19, v4, s[12:13] offset:36
	global_load_dword v20, v4, s[12:13] offset:96
	global_load_dword v21, v4, s[12:13] offset:108
	global_load_dword v22, v4, s[12:13] offset:120
	global_load_dword v23, v4, s[12:13] offset:132
	s_or_b64 exec, exec, s[14:15]
	s_movk_i32 s16, 0x7fff
	s_mov_b32 s17, 0x7060302
	s_waitcnt vmcnt(7)
	v_bfe_u32 v24, v16, 16, 1
	s_waitcnt vmcnt(6)
	v_bfe_u32 v25, v17, 16, 1
	s_waitcnt vmcnt(5)
	v_bfe_u32 v26, v18, 16, 1
	s_waitcnt vmcnt(4)
	v_bfe_u32 v27, v19, 16, 1
	s_waitcnt vmcnt(3)
	v_bfe_u32 v28, v20, 16, 1
	s_waitcnt vmcnt(2)
	v_bfe_u32 v29, v21, 16, 1
	s_waitcnt vmcnt(1)
	v_bfe_u32 v30, v22, 16, 1
	s_waitcnt vmcnt(0)
	v_bfe_u32 v31, v23, 16, 1
	v_add3_u32 v16, v16, v24, s16
	v_add3_u32 v17, v17, v25, s16
	v_add3_u32 v18, v18, v26, s16
	v_add3_u32 v19, v19, v27, s16
	v_add3_u32 v20, v20, v28, s16
	v_add3_u32 v21, v21, v29, s16
	v_add3_u32 v22, v22, v30, s16
	v_add3_u32 v23, v23, v31, s16
	v_perm_b32 v0, v17, v16, s17
	v_perm_b32 v1, v19, v18, s17
	v_perm_b32 v2, v21, v20, s17
	v_perm_b32 v3, v23, v22, s17
	global_store_dwordx4 v5, v[0:3], s[6:7]
	s_endpgm
.Lw2bf:
	s_load_dwordx2 s[12:13], s[0:1], 0x18
	s_sub_u32 s10, s10, 48
	s_and_b32 s11, s10, 3
	s_lshr_b32 s10, s10, 2
	s_lshl_b32 s10, s10, 13
	s_lshl_b32 s11, s11, 7
	s_add_u32 s10, s10, s11
	v_lshlrev_b32_e32 v4, 11, v3
	v_lshl_add_u32 v4, v2, 2, v4
	v_add_u32_e32 v4, s10, v4
	v_add_u32_e32 v6, 0x1000, v4
	v_add_u32_e32 v5, 0xfffff400, v7
	v_lshlrev_b32_e32 v5, 4, v5
	v_add_u32_e32 v5, 0xc000, v5
	s_waitcnt lgkmcnt(0)
	global_load_dword v16, v4, s[12:13] offset:0
	global_load_dword v17, v4, s[12:13] offset:512
	global_load_dword v18, v4, s[12:13] offset:1024
	global_load_dword v19, v4, s[12:13] offset:1536
	global_load_dword v20, v6, s[12:13] offset:0
	global_load_dword v21, v6, s[12:13] offset:512
	global_load_dword v22, v6, s[12:13] offset:1024
	global_load_dword v23, v6, s[12:13] offset:1536
	s_movk_i32 s16, 0x7fff
	s_mov_b32 s17, 0x7060302
	s_waitcnt vmcnt(7)
	v_bfe_u32 v24, v16, 16, 1
	s_waitcnt vmcnt(6)
	v_bfe_u32 v25, v17, 16, 1
	s_waitcnt vmcnt(5)
	v_bfe_u32 v26, v18, 16, 1
	s_waitcnt vmcnt(4)
	v_bfe_u32 v27, v19, 16, 1
	s_waitcnt vmcnt(3)
	v_bfe_u32 v28, v20, 16, 1
	s_waitcnt vmcnt(2)
	v_bfe_u32 v29, v21, 16, 1
	s_waitcnt vmcnt(1)
	v_bfe_u32 v30, v22, 16, 1
	s_waitcnt vmcnt(0)
	v_bfe_u32 v31, v23, 16, 1
	v_add3_u32 v16, v16, v24, s16
	v_add3_u32 v17, v17, v25, s16
	v_add3_u32 v18, v18, v26, s16
	v_add3_u32 v19, v19, v27, s16
	v_add3_u32 v20, v20, v28, s16
	v_add3_u32 v21, v21, v29, s16
	v_add3_u32 v22, v22, v30, s16
	v_add3_u32 v23, v23, v31, s16
	v_perm_b32 v0, v17, v16, s17
	v_perm_b32 v1, v19, v18, s17
	v_perm_b32 v2, v21, v20, s17
	v_perm_b32 v3, v23, v22, s17
	global_store_dwordx4 v5, v[0:3], s[6:7]
	s_endpgm
.Lw1f8:
	v_lshrrev_b32_e32 v1, 6, v7
	v_and_b32_e32 v2, 31, v0
	v_bfe_u32 v3, v0, 5, 1
	v_lshlrev_b32_e32 v5, 4, v7
	v_readfirstlane_b32 s10, v1
	v_cmp_ne_u32_e32 vcc, 0, v3
	s_and_b32 s11, s10, 1
	s_bfe_u32 s12, s10, 0x20001
	s_lshr_b32 s13, s10, 3
	s_lshl_b32 s13, s13, 2
	s_lshl1_add_u32 s16, s11, s13
	s_add_u32 s17, s16, 1
	s_lshl_b32 s12, s12, 7
	v_lshl_add_u32 v4, v2, 2, s12
	s_waitcnt lgkmcnt(0)
	s_lshl2_add_u32 s20, s16, 0x16
	s_mov_b32 s21, 0xa800
	s_mov_b32 s22, 0x41800000
	s_mov_b32 s23, 0x41800000
	s_cmp_eq_u32 s16, 0
	s_cselect_b32 s20, 0x0, s20
	s_cselect_b32 s21, 0x1c00, s21
	s_cmp_eq_u32 s16, 22
	s_cselect_b32 s22, 0, s22
	s_cselect_b32 s23, 0, s23
	s_lshl_b32 s20, s20, 9
	v_mad_u32_u24 v6, v3, s21, v4
	v_add_u32_e32 v6, s20, v6
	v_mov_b32_e32 v32, s22
	v_mov_b32_e32 v8, s23
	global_load_dword v16, v6, s[8:9]
	v_cndmask_b32_e32 v32, v32, v8, vcc
	s_lshl2_add_u32 s20, s16, 0xb8
	s_mov_b32 s21, 0xa800
	s_mov_b32 s22, 0x41000000
	s_mov_b32 s23, 0x41000000
	s_cmp_eq_u32 s16, 0
	s_cselect_b32 s20, 0x1, s20
	s_cselect_b32 s21, 0x1c00, s21
	s_cselect_b32 s22, 0x41800000, s22
	s_cselect_b32 s23, 0x41800000, s23
	s_cmp_eq_u32 s16, 22
	s_cselect_b32 s22, 0, s22
	s_cselect_b32 s23, 0, s23
	s_lshl_b32 s20, s20, 9
	v_mad_u32_u24 v6, v3, s21, v4
	v_add_u32_e32 v6, s20, v6
	v_mov_b32_e32 v33, s22
	v_mov_b32_e32 v8, s23
	global_load_dword v17, v6, s[8:9]
	v_cndmask_b32_e32 v33, v33, v8, vcc
	s_lshl2_add_u32 s20, s16, 0x17
	s_mov_b32 s21, 0xa800
	s_mov_b32 s22, 0x41800000
	s_mov_b32 s23, 0x41800000
	s_cmp_eq_u32 s16, 0
	s_cselect_b32 s20, 0x2, s20
	s_cselect_b32 s21, 0x1c00, s21
	s_cmp_eq_u32 s16, 22
	s_cselect_b32 s22, 0, s22
	s_cselect_b32 s23, 0, s23
	s_lshl_b32 s20, s20, 9
	v_mad_u32_u24 v6, v3, s21, v4
	v_add_u32_e32 v6, s20, v6
	v_mov_b32_e32 v34, s22
	v_mov_b32_e32 v8, s23
	global_load_dword v18, v6, s[8:9]
	v_cndmask_b32_e32 v34, v34, v8, vcc
	s_lshl2_add_u32 s20, s16, 0xb9
	s_mov_b32 s21, 0xa800
	s_mov_b32 s22, 0x41000000
	s_mov_b32 s23, 0x41000000
	s_cmp_eq_u32 s16, 0
	s_cselect_b32 s20, 0x3, s20
	s_cselect_b32 s21, 0x1c00, s21
	s_cselect_b32 s22, 0x41800000, s22
	s_cselect_b32 s23, 0x41800000, s23
	s_cmp_eq_u32 s16, 22
	s_cselect_b32 s22, 0, s22
	s_cselect_b32 s23, 0, s23
	s_lshl_b32 s20, s20, 9
	v_mad_u32_u24 v6, v3, s21, v4
	v_add_u32_e32 v6, s20, v6
	v_mov_b32_e32 v35, s22
	v_mov_b32_e32 v8, s23
	global_load_dword v19, v6, s[8:9]
	v_cndmask_b32_e32 v35, v35, v8, vcc
	s_lshl2_add_u32 s20, s16, 0x18
	s_mov_b32 s21, 0xa800
	s_mov_b32 s22, 0x41800000
	s_mov_b32 s23, 0x41800000
	s_cmp_eq_u32 s16, 0
	s_cselect_b32 s20, 0x4, s20
	s_cselect_b32 s21, 0x1c00, s21
	s_cmp_eq_u32 s16, 22
	s_cselect_b32 s22, 0, s22
	s_cselect_b32 s23, 0, s23
	s_lshl_b32 s20, s20, 9
	v_mad_u32_u24 v6, v3, s21, v4
	v_add_u32_e32 v6, s20, v6
	v_mov_b32_e32 v36, s22
	v_mov_b32_e32 v8, s23
	global_load_dword v20, v6, s[8:9]
	v_cndmask_b32_e32 v36, v36, v8, vcc
	s_lshl2_add_u32 s20, s16, 0xba
	s_mov_b32 s21, 0xa800
	s_mov_b32 s22, 0x41000000
	s_mov_b32 s23, 0x41000000
	s_cmp_eq_u32 s16, 0
	s_cselect_b32 s20, 0x5, s20
	s_cselect_b32 s21, 0x1c00, s21
	s_cselect_b32 s22, 0x41800000, s22
	s_cselect_b32 s23, 0x41800000, s23
	s_cmp_eq_u32 s16, 22
	s_cselect_b32 s22, 0, s22
	s_cselect_b32 s23, 0, s23
	s_lshl_b32 s20, s20, 9
	v_mad_u32_u24 v6, v3, s21, v4
	v_add_u32_e32 v6, s20, v6
	v_mov_b32_e32 v37, s22
	v_mov_b32_e32 v8, s23
	global_load_dword v21, v6, s[8:9]
	v_cndmask_b32_e32 v37, v37, v8, vcc
	s_lshl2_add_u32 s20, s16, 0x19
	s_mov_b32 s21, 0xa800
	s_mov_b32 s22, 0x41800000
	s_mov_b32 s23, 0x41800000
	s_cmp_eq_u32 s16, 0
	s_cselect_b32 s20, 0x6, s20
	s_cselect_b32 s21, 0x1c00, s21
	s_cmp_eq_u32 s16, 22
	s_cselect_b32 s22, 0, s22
	s_cselect_b32 s23, 0, s23
	s_lshl_b32 s20, s20, 9
	v_mad_u32_u24 v6, v3, s21, v4
	v_add_u32_e32 v6, s20, v6
	v_mov_b32_e32 v38, s22
	v_mov_b32_e32 v8, s23
	global_load_dword v22, v6, s[8:9]
	v_cndmask_b32_e32 v38, v38, v8, vcc
	s_lshl2_add_u32 s20, s16, 0xbb
	s_mov_b32 s21, 0xa800
	s_mov_b32 s22, 0x41000000
	s_mov_b32 s23, 0x41000000
	s_cmp_eq_u32 s16, 0
	s_cselect_b32 s20, 0x7, s20
	s_cselect_b32 s21, 0x1c00, s21
	s_cselect_b32 s22, 0x41800000, s22
	s_cselect_b32 s23, 0x41800000, s23
	s_cmp_eq_u32 s16, 22
	s_cselect_b32 s22, 0, s22
	s_cselect_b32 s23, 0, s23
	s_lshl_b32 s20, s20, 9
	v_mad_u32_u24 v6, v3, s21, v4
	v_add_u32_e32 v6, s20, v6
	v_mov_b32_e32 v39, s22
	v_mov_b32_e32 v8, s23
	global_load_dword v23, v6, s[8:9]
	v_cndmask_b32_e32 v39, v39, v8, vcc
	s_lshl2_add_u32 s20, s17, 0x16
	s_mov_b32 s21, 0xa800
	s_mov_b32 s22, 0x41800000
	s_mov_b32 s23, 0x41800000
	s_cmp_eq_u32 s16, 0
	s_cselect_b32 s20, 0x8, s20
	s_cselect_b32 s21, 0x1c00, s21
	s_cmp_eq_u32 s16, 22
	s_cselect_b32 s22, 0, s22
	s_cselect_b32 s23, 0, s23
	s_lshl_b32 s20, s20, 9
	v_mad_u32_u24 v6, v3, s21, v4
	v_add_u32_e32 v6, s20, v6
	v_mov_b32_e32 v40, s22
	v_mov_b32_e32 v8, s23
	global_load_dword v24, v6, s[8:9]
	v_cndmask_b32_e32 v40, v40, v8, vcc
	s_lshl2_add_u32 s20, s17, 0xb8
	s_mov_b32 s21, 0xa800
	s_mov_b32 s22, 0x41000000
	s_mov_b32 s23, 0x41000000
	s_cmp_eq_u32 s16, 0
	s_cselect_b32 s20, 0x9, s20
	s_cselect_b32 s21, 0x1c00, s21
	s_cselect_b32 s22, 0x41800000, s22
	s_cselect_b32 s23, 0x41800000, s23
	s_cmp_eq_u32 s16, 22
	s_cselect_b32 s22, 0, s22
	s_cselect_b32 s23, 0, s23
	s_lshl_b32 s20, s20, 9
	v_mad_u32_u24 v6, v3, s21, v4
	v_add_u32_e32 v6, s20, v6
	v_mov_b32_e32 v41, s22
	v_mov_b32_e32 v8, s23
	global_load_dword v25, v6, s[8:9]
	v_cndmask_b32_e32 v41, v41, v8, vcc
	s_lshl2_add_u32 s20, s17, 0x17
	s_mov_b32 s21, 0xa800
	s_mov_b32 s22, 0x41800000
	s_mov_b32 s23, 0x41800000
	s_cmp_eq_u32 s16, 0
	s_cselect_b32 s20, 0xa, s20
	s_cselect_b32 s21, 0x1c00, s21
	s_cmp_eq_u32 s16, 22
	s_cselect_b32 s22, 0, s22
	s_cselect_b32 s23, 0, s23
	s_lshl_b32 s20, s20, 9
	v_mad_u32_u24 v6, v3, s21, v4
	v_add_u32_e32 v6, s20, v6
	v_mov_b32_e32 v42, s22
	v_mov_b32_e32 v8, s23
	global_load_dword v26, v6, s[8:9]
	v_cndmask_b32_e32 v42, v42, v8, vcc
	s_lshl2_add_u32 s20, s17, 0xb9
	s_mov_b32 s21, 0xa800
	s_mov_b32 s22, 0x41000000
	s_mov_b32 s23, 0x41000000
	s_cmp_eq_u32 s16, 0
	s_cselect_b32 s20, 0xb, s20
	s_cselect_b32 s21, 0x1c00, s21
	s_cselect_b32 s22, 0x41800000, s22
	s_cselect_b32 s23, 0x41800000, s23
	s_cmp_eq_u32 s16, 22
	s_cselect_b32 s22, 0, s22
	s_cselect_b32 s23, 0, s23
	s_lshl_b32 s20, s20, 9
	v_mad_u32_u24 v6, v3, s21, v4
	v_add_u32_e32 v6, s20, v6
	v_mov_b32_e32 v43, s22
	v_mov_b32_e32 v8, s23
	global_load_dword v27, v6, s[8:9]
	v_cndmask_b32_e32 v43, v43, v8, vcc
	s_lshl2_add_u32 s20, s17, 0x18
	s_mov_b32 s21, 0xa800
	s_mov_b32 s22, 0x41800000
	s_mov_b32 s23, 0x41800000
	s_cmp_eq_u32 s16, 0
	s_cselect_b32 s20, 0xc, s20
	s_cselect_b32 s21, 0x1c00, s21
	s_cmp_eq_u32 s16, 20
	s_cselect_b32 s20, 0x6f, s20
	s_cselect_b32 s21, 0x14400, s21
	s_cselect_b32 s23, 0x41000000, s23
	s_cmp_eq_u32 s16, 22
	s_cselect_b32 s22, 0, s22
	s_cselect_b32 s23, 0, s23
	s_lshl_b32 s20, s20, 9
	v_mad_u32_u24 v6, v3, s21, v4
	v_add_u32_e32 v6, s20, v6
	v_mov_b32_e32 v44, s22
	v_mov_b32_e32 v8, s23
	global_load_dword v28, v6, s[8:9]
	v_cndmask_b32_e32 v44, v44, v8, vcc
	s_lshl2_add_u32 s20, s17, 0xba
	s_mov_b32 s21, 0xa800
	s_mov_b32 s22, 0x41000000
	s_mov_b32 s23, 0x41000000
	s_cmp_eq_u32 s16, 0
	s_cselect_b32 s20, 0x6c, s20
	s_cselect_b32 s21, 0x14400, s21
	s_cselect_b32 s22, 0x41800000, s22
	s_cmp_eq_u32 s16, 20
	s_cselect_b32 s20, 0x70, s20
	s_cselect_b32 s21, 0x14400, s21
	s_cselect_b32 s22, 0x41800000, s22
	s_cmp_eq_u32 s16, 22
	s_cselect_b32 s22, 0, s22
	s_cselect_b32 s23, 0, s23
	s_lshl_b32 s20, s20, 9
	v_mad_u32_u24 v6, v3, s21, v4
	v_add_u32_e32 v6, s20, v6
	v_mov_b32_e32 v45, s22
	v_mov_b32_e32 v8, s23
	global_load_dword v29, v6, s[8:9]
	v_cndmask_b32_e32 v45, v45, v8, vcc
	s_lshl2_add_u32 s20, s17, 0x19
	s_mov_b32 s21, 0xa800
	s_mov_b32 s22, 0x41800000
	s_mov_b32 s23, 0x41800000
	s_cmp_eq_u32 s16, 0
	s_cselect_b32 s20, 0x6d, s20
	s_cselect_b32 s21, 0x14400, s21
	s_cselect_b32 s23, 0x41000000, s23
	s_cmp_eq_u32 s16, 20
	s_cselect_b32 s20, 0x71, s20
	s_cselect_b32 s21, 0x14400, s21
	s_cselect_b32 s23, 0x41000000, s23
	s_cmp_eq_u32 s16, 22
	s_cselect_b32 s22, 0, s22
	s_cselect_b32 s23, 0, s23
	s_lshl_b32 s20, s20, 9
	v_mad_u32_u24 v6, v3, s21, v4
	v_add_u32_e32 v6, s20, v6
	v_mov_b32_e32 v46, s22
	v_mov_b32_e32 v8, s23
	global_load_dword v30, v6, s[8:9]
	v_cndmask_b32_e32 v46, v46, v8, vcc
	s_lshl2_add_u32 s20, s17, 0xbb
	s_mov_b32 s21, 0xa800
	s_mov_b32 s22, 0x41000000
	s_mov_b32 s23, 0x41000000
	s_cmp_eq_u32 s16, 0
	s_cselect_b32 s20, 0x6e, s20
	s_cselect_b32 s21, 0x14400, s21
	s_cselect_b32 s22, 0x41800000, s22
	s_cmp_eq_u32 s16, 20
	s_cselect_b32 s20, 0xd, s20
	s_cselect_b32 s21, 0x0, s21
	s_cselect_b32 s22, 0x41800000, s22
	s_cselect_b32 s23, 0x0, s23
	s_cmp_eq_u32 s16, 22
	s_cselect_b32 s22, 0, s22
	s_cselect_b32 s23, 0, s23
	s_lshl_b32 s20, s20, 9
	v_mad_u32_u24 v6, v3, s21, v4
	v_add_u32_e32 v6, s20, v6
	v_mov_b32_e32 v47, s22
	v_mov_b32_e32 v8, s23
	global_load_dword v31, v6, s[8:9]
	v_cndmask_b32_e32 v47, v47, v8, vcc
	s_waitcnt vmcnt(15)
	v_mul_f32_e32 v16, v16, v32
	s_waitcnt vmcnt(14)
	v_mul_f32_e32 v17, v17, v33
	s_waitcnt vmcnt(13)
	v_mul_f32_e32 v18, v18, v34
	s_waitcnt vmcnt(12)
	v_mul_f32_e32 v19, v19, v35
	s_waitcnt vmcnt(11)
	v_mul_f32_e32 v20, v20, v36
	s_waitcnt vmcnt(10)
	v_mul_f32_e32 v21, v21, v37
	s_waitcnt vmcnt(9)
	v_mul_f32_e32 v22, v22, v38
	s_waitcnt vmcnt(8)
	v_mul_f32_e32 v23, v23, v39
	s_waitcnt vmcnt(7)
	v_mul_f32_e32 v24, v24, v40
	s_waitcnt vmcnt(6)
	v_mul_f32_e32 v25, v25, v41
	s_waitcnt vmcnt(5)
	v_mul_f32_e32 v26, v26, v42
	s_waitcnt vmcnt(4)
	v_mul_f32_e32 v27, v27, v43
	s_waitcnt vmcnt(3)
	v_mul_f32_e32 v28, v28, v44
	s_waitcnt vmcnt(2)
	v_mul_f32_e32 v29, v29, v45
	s_waitcnt vmcnt(1)
	v_mul_f32_e32 v30, v30, v46
	s_waitcnt vmcnt(0)
	v_mul_f32_e32 v31, v31, v47
	v_cvt_pk_fp8_f32 v0, v16, v17
	v_cvt_pk_fp8_f32 v1, v20, v21
	v_cvt_pk_fp8_f32 v2, v24, v25
	v_cvt_pk_fp8_f32 v3, v28, v29
	v_cvt_pk_fp8_f32 v0, v18, v19 op_sel:[0,0,1]
	v_cvt_pk_fp8_f32 v1, v22, v23 op_sel:[0,0,1]
	v_cvt_pk_fp8_f32 v2, v26, v27 op_sel:[0,0,1]
	v_cvt_pk_fp8_f32 v3, v30, v31 op_sel:[0,0,1]
	s_nop 1
	global_store_dwordx4 v5, v[0:3], s[6:7]
	s_endpgm
